# speedup vs baseline: 1.0085x; 1.0085x over previous
_Z12carry_kernelPKDv2_DF16_PDF16_:
	s_load_dwordx4 s[4:7], s[0:1], 0x0
	s_lshl_b32 s1, s2, 1
	s_mul_hi_u32 s3, s2, 0xaaaaaaab
	s_lshr_b32 s0, s2, 3
	s_and_b32 s1, s1, 12
	s_lshr_b32 s3, s3, 4
	s_add_i32 s1, s1, s3
	s_mul_hi_u32 s3, s0, 0x55555556
	s_mul_i32 s3, s3, 3
	s_sub_i32 s0, s0, s3
	s_mul_i32 s1, s1, 6
	s_lshl_b32 s0, s0, 1
	s_add_i32 s1, s1, s0
	s_and_b32 s0, s2, 1
	s_or_b32 s8, s1, s0
	s_mul_hi_u32 s0, s1, 0xaaaaaaab
	s_lshr_b32 s0, s0, 2
	s_bitcmp0_b32 s0, 1
	s_mov_b32 s9, 0
	s_cselect_b64 vcc, -1, 0
	s_lshl_b64 s[0:1], s[8:9], 17
	v_and_b32_e32 v1, 31, v0
	s_waitcnt lgkmcnt(0)
	s_add_u32 s0, s4, s0
	s_addc_u32 s1, s5, s1
	v_lshlrev_b32_e32 v2, 2, v1
	v_mov_b32_e32 v3, 0
	v_and_b32_e32 v56, 0x3e0, v0
	v_sub_u32_e32 v7, 0x3ff, v56
	v_cndmask_b32_e32 v7, v7, v56, vcc
	v_mov_b32_e32 v71, 0xffffff80
	v_mov_b32_e32 v72, 0x80
	v_cndmask_b32_e32 v71, v71, v72, vcc
	v_lshl_add_u32 v70, v7, 7, v2
	v_lshlrev_b32_e32 v90, 1, v1
	v_lshl_add_u32 v90, v7, 6, v90
	v_ashrrev_i32_e32 v91, 1, v71
	global_load_dword v69, v70, s[0:1]
	v_add_u32_e32 v70, v70, v71
	global_load_dword v68, v70, s[0:1]
	v_add_u32_e32 v70, v70, v71
	global_load_dword v67, v70, s[0:1]
	v_add_u32_e32 v70, v70, v71
	global_load_dword v66, v70, s[0:1]
	v_add_u32_e32 v70, v70, v71
	global_load_dword v65, v70, s[0:1]
	v_add_u32_e32 v70, v70, v71
	global_load_dword v64, v70, s[0:1]
	v_add_u32_e32 v70, v70, v71
	global_load_dword v63, v70, s[0:1]
	v_add_u32_e32 v70, v70, v71
	global_load_dword v62, v70, s[0:1]
	v_add_u32_e32 v70, v70, v71
	global_load_dword v61, v70, s[0:1]
	v_add_u32_e32 v70, v70, v71
	global_load_dword v60, v70, s[0:1]
	v_add_u32_e32 v70, v70, v71
	global_load_dword v59, v70, s[0:1]
	v_add_u32_e32 v70, v70, v71
	global_load_dword v58, v70, s[0:1]
	v_add_u32_e32 v70, v70, v71
	global_load_dword v25, v70, s[0:1]
	v_add_u32_e32 v70, v70, v71
	global_load_dword v24, v70, s[0:1]
	v_add_u32_e32 v70, v70, v71
	global_load_dword v23, v70, s[0:1]
	v_add_u32_e32 v70, v70, v71
	global_load_dword v22, v70, s[0:1]
	v_add_u32_e32 v70, v70, v71
	global_load_dword v21, v70, s[0:1]
	v_add_u32_e32 v70, v70, v71
	global_load_dword v20, v70, s[0:1]
	v_add_u32_e32 v70, v70, v71
	global_load_dword v19, v70, s[0:1]
	v_add_u32_e32 v70, v70, v71
	global_load_dword v18, v70, s[0:1]
	v_add_u32_e32 v70, v70, v71
	global_load_dword v17, v70, s[0:1]
	v_add_u32_e32 v70, v70, v71
	global_load_dword v16, v70, s[0:1]
	v_add_u32_e32 v70, v70, v71
	global_load_dword v15, v70, s[0:1]
	v_add_u32_e32 v70, v70, v71
	global_load_dword v14, v70, s[0:1]
	v_add_u32_e32 v70, v70, v71
	global_load_dword v13, v70, s[0:1]
	v_add_u32_e32 v70, v70, v71
	global_load_dword v12, v70, s[0:1]
	v_add_u32_e32 v70, v70, v71
	global_load_dword v11, v70, s[0:1]
	v_add_u32_e32 v70, v70, v71
	global_load_dword v10, v70, s[0:1]
	v_add_u32_e32 v70, v70, v71
	global_load_dword v9, v70, s[0:1]
	v_add_u32_e32 v70, v70, v71
	global_load_dword v8, v70, s[0:1]
	v_add_u32_e32 v70, v70, v71
	global_load_dword v6, v70, s[0:1]
	v_add_u32_e32 v70, v70, v71
	global_load_dword v4, v70, s[0:1]
	s_waitcnt vmcnt(31)
	v_cvt_f32_f16_e32 v57, v69
	s_waitcnt vmcnt(30)
	v_cvt_f32_f16_e32 v72, v68
	s_waitcnt vmcnt(29)
	v_cvt_f32_f16_e32 v73, v67
	v_lshrrev_b32_e32 v0, 5, v0
	s_movk_i32 s0, 0x84
	v_mul_f32_e32 v5, v57, v72
	v_mul_f32_e32 v5, v5, v73
	v_mad_u32_u24 v2, v0, s0, v2
	v_lshlrev_b32_e32 v0, 2, v0
	s_waitcnt vmcnt(28)
	v_cvt_f32_f16_e32 v57, v66
	s_waitcnt vmcnt(27)
	v_cvt_f32_f16_e32 v70, v65
	s_waitcnt vmcnt(26)
	v_cvt_f32_f16_e32 v71, v64
	s_waitcnt vmcnt(25)
	v_cvt_f32_f16_e32 v72, v63
	v_mul_f32_e32 v5, v5, v57
	v_mul_f32_e32 v5, v5, v70
	v_mul_f32_e32 v5, v5, v71
	v_mul_f32_e32 v5, v5, v72
	v_mad_u32_u24 v0, v1, s0, v0
	s_waitcnt vmcnt(24)
	v_cvt_f32_f16_e32 v57, v62
	s_waitcnt vmcnt(23)
	v_cvt_f32_f16_e32 v70, v61
	s_waitcnt vmcnt(22)
	v_cvt_f32_f16_e32 v71, v60
	s_waitcnt vmcnt(21)
	v_cvt_f32_f16_e32 v72, v59
	v_mul_f32_e32 v5, v5, v57
	s_waitcnt vmcnt(20)
	v_cvt_f32_f16_e32 v57, v58
	v_mul_f32_e32 v5, v5, v70
	s_waitcnt vmcnt(19)
	v_cvt_f32_f16_e32 v70, v25
	v_mul_f32_e32 v5, v5, v71
	s_waitcnt vmcnt(18)
	v_cvt_f32_f16_e32 v71, v24
	v_mul_f32_e32 v5, v5, v72
	s_waitcnt vmcnt(17)
	v_cvt_f32_f16_e32 v72, v23
	v_mul_f32_e32 v5, v5, v57
	s_waitcnt vmcnt(16)
	v_cvt_f32_f16_e32 v57, v22
	v_mul_f32_e32 v5, v5, v70
	s_waitcnt vmcnt(15)
	v_cvt_f32_f16_e32 v70, v21
	v_mul_f32_e32 v5, v5, v71
	s_waitcnt vmcnt(14)
	v_cvt_f32_f16_e32 v71, v20
	v_mul_f32_e32 v5, v5, v72
	s_waitcnt vmcnt(13)
	v_cvt_f32_f16_e32 v72, v19
	v_mul_f32_e32 v5, v5, v57
	s_waitcnt vmcnt(12)
	v_cvt_f32_f16_e32 v57, v18
	v_mul_f32_e32 v5, v5, v70
	s_waitcnt vmcnt(11)
	v_cvt_f32_f16_e32 v70, v17
	v_mul_f32_e32 v5, v5, v71
	s_waitcnt vmcnt(10)
	v_cvt_f32_f16_e32 v71, v16
	v_mul_f32_e32 v5, v5, v72
	s_waitcnt vmcnt(9)
	v_cvt_f32_f16_e32 v72, v15
	v_mul_f32_e32 v5, v5, v57
	s_waitcnt vmcnt(8)
	v_cvt_f32_f16_e32 v57, v14
	v_mul_f32_e32 v5, v5, v70
	s_waitcnt vmcnt(7)
	v_cvt_f32_f16_e32 v70, v13
	v_mul_f32_e32 v5, v5, v71
	s_waitcnt vmcnt(6)
	v_cvt_f32_f16_e32 v71, v12
	v_mul_f32_e32 v5, v5, v72
	s_waitcnt vmcnt(5)
	v_cvt_f32_f16_e32 v72, v11
	v_mul_f32_e32 v5, v5, v57
	s_waitcnt vmcnt(4)
	v_cvt_f32_f16_e32 v57, v10
	v_mul_f32_e32 v5, v5, v70
	v_mul_f32_e32 v5, v5, v71
	v_mul_f32_e32 v5, v5, v72
	v_mul_f32_e32 v5, v5, v57
	v_fma_mix_f32 v57, v69, 0, v69 op_sel:[0,0,1] op_sel_hi:[1,0,1]
	s_waitcnt vmcnt(3)
	v_cvt_f32_f16_e32 v70, v9
	v_fma_mix_f32 v57, v57, v68, v68 op_sel:[0,0,1] op_sel_hi:[0,1,1]
	v_fma_mix_f32 v57, v57, v67, v67 op_sel:[0,0,1] op_sel_hi:[0,1,1]
	v_fma_mix_f32 v57, v57, v66, v66 op_sel:[0,0,1] op_sel_hi:[0,1,1]
	v_fma_mix_f32 v57, v57, v65, v65 op_sel:[0,0,1] op_sel_hi:[0,1,1]
	v_fma_mix_f32 v57, v57, v64, v64 op_sel:[0,0,1] op_sel_hi:[0,1,1]
	v_fma_mix_f32 v57, v57, v63, v63 op_sel:[0,0,1] op_sel_hi:[0,1,1]
	v_fma_mix_f32 v57, v57, v62, v62 op_sel:[0,0,1] op_sel_hi:[0,1,1]
	v_fma_mix_f32 v57, v57, v61, v61 op_sel:[0,0,1] op_sel_hi:[0,1,1]
	v_fma_mix_f32 v57, v57, v60, v60 op_sel:[0,0,1] op_sel_hi:[0,1,1]
	v_fma_mix_f32 v57, v57, v59, v59 op_sel:[0,0,1] op_sel_hi:[0,1,1]
	v_fma_mix_f32 v57, v57, v58, v58 op_sel:[0,0,1] op_sel_hi:[0,1,1]
	v_fma_mix_f32 v57, v57, v25, v25 op_sel:[0,0,1] op_sel_hi:[0,1,1]
	v_fma_mix_f32 v57, v57, v24, v24 op_sel:[0,0,1] op_sel_hi:[0,1,1]
	v_fma_mix_f32 v57, v57, v23, v23 op_sel:[0,0,1] op_sel_hi:[0,1,1]
	v_fma_mix_f32 v57, v57, v22, v22 op_sel:[0,0,1] op_sel_hi:[0,1,1]
	v_fma_mix_f32 v57, v57, v21, v21 op_sel:[0,0,1] op_sel_hi:[0,1,1]
	v_fma_mix_f32 v57, v57, v20, v20 op_sel:[0,0,1] op_sel_hi:[0,1,1]
	v_fma_mix_f32 v57, v57, v19, v19 op_sel:[0,0,1] op_sel_hi:[0,1,1]
	v_fma_mix_f32 v57, v57, v18, v18 op_sel:[0,0,1] op_sel_hi:[0,1,1]
	v_fma_mix_f32 v57, v57, v17, v17 op_sel:[0,0,1] op_sel_hi:[0,1,1]
	v_fma_mix_f32 v57, v57, v16, v16 op_sel:[0,0,1] op_sel_hi:[0,1,1]
	v_fma_mix_f32 v57, v57, v15, v15 op_sel:[0,0,1] op_sel_hi:[0,1,1]
	v_fma_mix_f32 v57, v57, v14, v14 op_sel:[0,0,1] op_sel_hi:[0,1,1]
	v_fma_mix_f32 v57, v57, v13, v13 op_sel:[0,0,1] op_sel_hi:[0,1,1]
	s_waitcnt vmcnt(2)
	v_cvt_f32_f16_e32 v71, v8
	v_fma_mix_f32 v57, v57, v12, v12 op_sel:[0,0,1] op_sel_hi:[0,1,1]
	s_waitcnt vmcnt(1)
	v_cvt_f32_f16_e32 v72, v6
	v_fma_mix_f32 v57, v57, v11, v11 op_sel:[0,0,1] op_sel_hi:[0,1,1]
	v_mul_f32_e32 v5, v5, v70
	v_fma_mix_f32 v57, v57, v10, v10 op_sel:[0,0,1] op_sel_hi:[0,1,1]
	s_waitcnt vmcnt(0)
	v_cvt_f32_f16_e32 v70, v4
	v_fma_mix_f32 v57, v57, v9, v9 op_sel:[0,0,1] op_sel_hi:[0,1,1]
	v_mul_f32_e32 v5, v5, v71
	v_fma_mix_f32 v57, v57, v8, v8 op_sel:[0,0,1] op_sel_hi:[0,1,1]
	v_mul_f32_e32 v5, v5, v72
	v_fma_mix_f32 v57, v57, v6, v6 op_sel:[0,0,1] op_sel_hi:[0,1,1]
	v_fma_mix_f32 v4, v57, v4, v4 op_sel:[0,0,1] op_sel_hi:[0,1,1]
	v_mul_f32_e32 v5, v5, v70
	ds_write_b32 v2, v5 offset:8448
	ds_write_b32 v2, v4 offset:4224
	v_mbcnt_lo_u32_b32 v4, -1, 0
	s_waitcnt lgkmcnt(0)
	s_barrier
	v_mbcnt_hi_u32_b32 v4, -1, v4
	ds_read_b32 v70, v0 offset:4224
	ds_read_b32 v71, v0 offset:8448
	v_and_b32_e32 v5, 0x60, v4
	v_add_u32_e32 v57, -1, v4
	v_cmp_lt_i32_e32 vcc, v57, v5
	v_add_u32_e32 v73, -2, v4
	v_cmp_lt_i32_e64 s[0:1], v73, v5
	v_cndmask_b32_e32 v57, v57, v4, vcc
	v_lshlrev_b32_e32 v57, 2, v57
	s_waitcnt lgkmcnt(1)
	ds_bpermute_b32 v72, v57, v70
	v_cmp_eq_u32_e32 vcc, 0, v1
	v_cndmask_b32_e64 v73, v73, v4, s[0:1]
	v_lshlrev_b32_e32 v73, 2, v73
	v_cmp_gt_u32_e64 s[0:1], 2, v1
	s_waitcnt lgkmcnt(0)
	v_fma_f32 v72, v71, v72, v70
	v_cndmask_b32_e32 v70, v72, v70, vcc
	ds_bpermute_b32 v72, v57, v71
	ds_bpermute_b32 v74, v73, v70
	s_waitcnt lgkmcnt(1)
	v_mul_f32_e32 v72, v71, v72
	v_cndmask_b32_e32 v71, v72, v71, vcc
	s_waitcnt lgkmcnt(0)
	v_fma_f32 v72, v71, v74, v70
	v_cndmask_b32_e64 v70, v72, v70, s[0:1]
	ds_bpermute_b32 v72, v73, v71
	v_add_u32_e32 v73, -4, v4
	v_cmp_lt_i32_e64 s[2:3], v73, v5
	s_waitcnt lgkmcnt(0)
	v_mul_f32_e32 v72, v71, v72
	v_cndmask_b32_e64 v73, v73, v4, s[2:3]
	v_lshlrev_b32_e32 v73, 2, v73
	ds_bpermute_b32 v74, v73, v70
	v_cndmask_b32_e64 v71, v72, v71, s[0:1]
	v_cmp_gt_u32_e64 s[0:1], 4, v1
	s_waitcnt lgkmcnt(0)
	v_fma_f32 v72, v71, v74, v70
	v_cndmask_b32_e64 v70, v72, v70, s[0:1]
	ds_bpermute_b32 v72, v73, v71
	v_add_u32_e32 v73, -8, v4
	v_cmp_lt_i32_e64 s[2:3], v73, v5
	s_waitcnt lgkmcnt(0)
	v_mul_f32_e32 v72, v71, v72
	v_cndmask_b32_e64 v73, v73, v4, s[2:3]
	v_lshlrev_b32_e32 v73, 2, v73
	ds_bpermute_b32 v74, v73, v70
	v_cndmask_b32_e64 v71, v72, v71, s[0:1]
	v_cmp_gt_u32_e64 s[0:1], 8, v1
	s_waitcnt lgkmcnt(0)
	v_fma_f32 v72, v71, v74, v70
	v_cndmask_b32_e64 v70, v72, v70, s[0:1]
	ds_bpermute_b32 v72, v73, v71
	v_add_u32_e32 v73, -16, v4
	v_cmp_lt_i32_e64 s[2:3], v73, v5
	s_waitcnt lgkmcnt(0)
	v_mul_f32_e32 v5, v71, v72
	v_cndmask_b32_e64 v4, v73, v4, s[2:3]
	v_lshlrev_b32_e32 v4, 2, v4
	ds_bpermute_b32 v4, v4, v70
	v_cndmask_b32_e64 v5, v5, v71, s[0:1]
	v_cmp_gt_u32_e64 s[0:1], 16, v1
	s_waitcnt lgkmcnt(0)
	v_fma_f32 v4, v5, v4, v70
	v_cndmask_b32_e64 v4, v4, v70, s[0:1]
	ds_bpermute_b32 v4, v57, v4
	s_lshl_b64 s[0:1], s[8:9], 16
	s_add_u32 s0, s6, s0
	s_addc_u32 s1, s7, s1
	s_waitcnt lgkmcnt(0)
	v_cndmask_b32_e64 v4, v4, 0, vcc
	ds_write_b32 v0, v4
	s_waitcnt lgkmcnt(0)
	s_barrier
	ds_read_b32 v57, v2
	s_waitcnt lgkmcnt(0)
	v_cvt_f16_f32_e32 v70, v57
	v_fma_mixlo_f16 v26, v57, v69, v69 op_sel:[0,0,1] op_sel_hi:[0,1,1]
	global_store_short v90, v70, s[0:1]
	v_add_u32_e32 v90, v90, v91
	global_store_short v90, v26, s[0:1]
	v_add_u32_e32 v90, v90, v91
	v_fma_mix_f32 v26, v57, v69, v69 op_sel:[0,0,1] op_sel_hi:[0,1,1]
	v_fma_mixlo_f16 v27, v26, v68, v68 op_sel:[0,0,1] op_sel_hi:[0,1,1]
	v_fma_mix_f32 v26, v26, v68, v68 op_sel:[0,0,1] op_sel_hi:[0,1,1]
	global_store_short v90, v27, s[0:1]
	v_add_u32_e32 v90, v90, v91
	v_fma_mixlo_f16 v27, v26, v67, v67 op_sel:[0,0,1] op_sel_hi:[0,1,1]
	v_fma_mix_f32 v26, v26, v67, v67 op_sel:[0,0,1] op_sel_hi:[0,1,1]
	global_store_short v90, v27, s[0:1]
	v_add_u32_e32 v90, v90, v91
	v_fma_mixlo_f16 v27, v26, v66, v66 op_sel:[0,0,1] op_sel_hi:[0,1,1]
	v_fma_mix_f32 v2, v26, v66, v66 op_sel:[0,0,1] op_sel_hi:[0,1,1]
	global_store_short v90, v27, s[0:1]
	v_add_u32_e32 v90, v90, v91
	v_fma_mix_f32 v26, v2, v65, v65 op_sel:[0,0,1] op_sel_hi:[0,1,1]
	v_fma_mixlo_f16 v27, v2, v65, v65 op_sel:[0,0,1] op_sel_hi:[0,1,1]
	global_store_short v90, v27, s[0:1]
	v_add_u32_e32 v90, v90, v91
	v_fma_mix_f32 v27, v26, v64, v64 op_sel:[0,0,1] op_sel_hi:[0,1,1]
	v_fma_mixlo_f16 v26, v26, v64, v64 op_sel:[0,0,1] op_sel_hi:[0,1,1]
	global_store_short v90, v26, s[0:1]
	v_add_u32_e32 v90, v90, v91
	v_fma_mix_f32 v26, v27, v63, v63 op_sel:[0,0,1] op_sel_hi:[0,1,1]
	v_fma_mixlo_f16 v27, v27, v63, v63 op_sel:[0,0,1] op_sel_hi:[0,1,1]
	global_store_short v90, v27, s[0:1]
	v_add_u32_e32 v90, v90, v91
	v_fma_mix_f32 v27, v26, v62, v62 op_sel:[0,0,1] op_sel_hi:[0,1,1]
	v_fma_mixlo_f16 v26, v26, v62, v62 op_sel:[0,0,1] op_sel_hi:[0,1,1]
	global_store_short v90, v26, s[0:1]
	v_add_u32_e32 v90, v90, v91
	v_fma_mix_f32 v26, v27, v61, v61 op_sel:[0,0,1] op_sel_hi:[0,1,1]
	v_fma_mixlo_f16 v27, v27, v61, v61 op_sel:[0,0,1] op_sel_hi:[0,1,1]
	global_store_short v90, v27, s[0:1]
	v_add_u32_e32 v90, v90, v91
	v_fma_mix_f32 v27, v26, v60, v60 op_sel:[0,0,1] op_sel_hi:[0,1,1]
	v_fma_mixlo_f16 v26, v26, v60, v60 op_sel:[0,0,1] op_sel_hi:[0,1,1]
	global_store_short v90, v26, s[0:1]
	v_add_u32_e32 v90, v90, v91
	v_fma_mix_f32 v26, v27, v59, v59 op_sel:[0,0,1] op_sel_hi:[0,1,1]
	v_fma_mixlo_f16 v27, v27, v59, v59 op_sel:[0,0,1] op_sel_hi:[0,1,1]
	global_store_short v90, v27, s[0:1]
	v_add_u32_e32 v90, v90, v91
	v_fma_mix_f32 v27, v26, v58, v58 op_sel:[0,0,1] op_sel_hi:[0,1,1]
	v_fma_mixlo_f16 v26, v26, v58, v58 op_sel:[0,0,1] op_sel_hi:[0,1,1]
	global_store_short v90, v26, s[0:1]
	v_add_u32_e32 v90, v90, v91
	v_fma_mix_f32 v26, v27, v25, v25 op_sel:[0,0,1] op_sel_hi:[0,1,1]
	v_fma_mixlo_f16 v25, v27, v25, v25 op_sel:[0,0,1] op_sel_hi:[0,1,1]
	global_store_short v90, v25, s[0:1]
	v_add_u32_e32 v90, v90, v91
	v_fma_mix_f32 v25, v26, v24, v24 op_sel:[0,0,1] op_sel_hi:[0,1,1]
	v_fma_mixlo_f16 v24, v26, v24, v24 op_sel:[0,0,1] op_sel_hi:[0,1,1]
	global_store_short v90, v24, s[0:1]
	v_add_u32_e32 v90, v90, v91
	v_fma_mix_f32 v24, v25, v23, v23 op_sel:[0,0,1] op_sel_hi:[0,1,1]
	v_fma_mixlo_f16 v23, v25, v23, v23 op_sel:[0,0,1] op_sel_hi:[0,1,1]
	global_store_short v90, v23, s[0:1]
	v_add_u32_e32 v90, v90, v91
	v_fma_mix_f32 v23, v24, v22, v22 op_sel:[0,0,1] op_sel_hi:[0,1,1]
	v_fma_mixlo_f16 v22, v24, v22, v22 op_sel:[0,0,1] op_sel_hi:[0,1,1]
	global_store_short v90, v22, s[0:1]
	v_add_u32_e32 v90, v90, v91
	v_fma_mix_f32 v22, v23, v21, v21 op_sel:[0,0,1] op_sel_hi:[0,1,1]
	v_fma_mixlo_f16 v21, v23, v21, v21 op_sel:[0,0,1] op_sel_hi:[0,1,1]
	global_store_short v90, v21, s[0:1]
	v_add_u32_e32 v90, v90, v91
	v_fma_mix_f32 v21, v22, v20, v20 op_sel:[0,0,1] op_sel_hi:[0,1,1]
	v_fma_mixlo_f16 v20, v22, v20, v20 op_sel:[0,0,1] op_sel_hi:[0,1,1]
	global_store_short v90, v20, s[0:1]
	v_add_u32_e32 v90, v90, v91
	v_fma_mix_f32 v20, v21, v19, v19 op_sel:[0,0,1] op_sel_hi:[0,1,1]
	v_fma_mixlo_f16 v19, v21, v19, v19 op_sel:[0,0,1] op_sel_hi:[0,1,1]
	global_store_short v90, v19, s[0:1]
	v_add_u32_e32 v90, v90, v91
	v_fma_mix_f32 v19, v20, v18, v18 op_sel:[0,0,1] op_sel_hi:[0,1,1]
	v_fma_mixlo_f16 v18, v20, v18, v18 op_sel:[0,0,1] op_sel_hi:[0,1,1]
	global_store_short v90, v18, s[0:1]
	v_add_u32_e32 v90, v90, v91
	v_fma_mix_f32 v18, v19, v17, v17 op_sel:[0,0,1] op_sel_hi:[0,1,1]
	v_fma_mixlo_f16 v17, v19, v17, v17 op_sel:[0,0,1] op_sel_hi:[0,1,1]
	global_store_short v90, v17, s[0:1]
	v_add_u32_e32 v90, v90, v91
	v_fma_mix_f32 v17, v18, v16, v16 op_sel:[0,0,1] op_sel_hi:[0,1,1]
	v_fma_mixlo_f16 v16, v18, v16, v16 op_sel:[0,0,1] op_sel_hi:[0,1,1]
	global_store_short v90, v16, s[0:1]
	v_add_u32_e32 v90, v90, v91
	v_fma_mix_f32 v16, v17, v15, v15 op_sel:[0,0,1] op_sel_hi:[0,1,1]
	v_fma_mixlo_f16 v15, v17, v15, v15 op_sel:[0,0,1] op_sel_hi:[0,1,1]
	global_store_short v90, v15, s[0:1]
	v_add_u32_e32 v90, v90, v91
	v_fma_mix_f32 v15, v16, v14, v14 op_sel:[0,0,1] op_sel_hi:[0,1,1]
	v_fma_mixlo_f16 v14, v16, v14, v14 op_sel:[0,0,1] op_sel_hi:[0,1,1]
	global_store_short v90, v14, s[0:1]
	v_add_u32_e32 v90, v90, v91
	v_fma_mix_f32 v14, v15, v13, v13 op_sel:[0,0,1] op_sel_hi:[0,1,1]
	v_fma_mixlo_f16 v13, v15, v13, v13 op_sel:[0,0,1] op_sel_hi:[0,1,1]
	global_store_short v90, v13, s[0:1]
	v_add_u32_e32 v90, v90, v91
	v_fma_mix_f32 v13, v14, v12, v12 op_sel:[0,0,1] op_sel_hi:[0,1,1]
	v_fma_mixlo_f16 v12, v14, v12, v12 op_sel:[0,0,1] op_sel_hi:[0,1,1]
	global_store_short v90, v12, s[0:1]
	v_add_u32_e32 v90, v90, v91
	v_fma_mix_f32 v12, v13, v11, v11 op_sel:[0,0,1] op_sel_hi:[0,1,1]
	v_fma_mixlo_f16 v11, v13, v11, v11 op_sel:[0,0,1] op_sel_hi:[0,1,1]
	global_store_short v90, v11, s[0:1]
	v_add_u32_e32 v90, v90, v91
	v_fma_mix_f32 v11, v12, v10, v10 op_sel:[0,0,1] op_sel_hi:[0,1,1]
	v_fma_mixlo_f16 v10, v12, v10, v10 op_sel:[0,0,1] op_sel_hi:[0,1,1]
	global_store_short v90, v10, s[0:1]
	v_add_u32_e32 v90, v90, v91
	v_fma_mix_f32 v10, v11, v9, v9 op_sel:[0,0,1] op_sel_hi:[0,1,1]
	v_fma_mixlo_f16 v9, v11, v9, v9 op_sel:[0,0,1] op_sel_hi:[0,1,1]
	global_store_short v90, v9, s[0:1]
	v_add_u32_e32 v90, v90, v91
	v_fma_mix_f32 v9, v10, v8, v8 op_sel:[0,0,1] op_sel_hi:[0,1,1]
	v_fma_mixlo_f16 v8, v10, v8, v8 op_sel:[0,0,1] op_sel_hi:[0,1,1]
	global_store_short v90, v8, s[0:1]
	v_add_u32_e32 v90, v90, v91
	v_fma_mixlo_f16 v4, v9, v6, v6 op_sel:[0,0,1] op_sel_hi:[0,1,1]
	global_store_short v90, v4, s[0:1]
	s_endpgm

	.amdhsa_kernel _Z12carry_kernelPKDv2_DF16_PDF16_
		.amdhsa_group_segment_fixed_size 12672
		.amdhsa_private_segment_fixed_size 0
		.amdhsa_kernarg_size 16
		.amdhsa_user_sgpr_count 2
		.amdhsa_user_sgpr_dispatch_ptr 0
		.amdhsa_user_sgpr_queue_ptr 0
		.amdhsa_user_sgpr_kernarg_segment_ptr 1
		.amdhsa_user_sgpr_dispatch_id 0
		.amdhsa_user_sgpr_kernarg_preload_length 0
		.amdhsa_user_sgpr_kernarg_preload_offset 0
		.amdhsa_user_sgpr_private_segment_size 0
		.amdhsa_uses_dynamic_stack 0
		.amdhsa_enable_private_segment 0
		.amdhsa_system_sgpr_workgroup_id_x 1
		.amdhsa_system_sgpr_workgroup_id_y 0
		.amdhsa_system_sgpr_workgroup_id_z 0
		.amdhsa_system_sgpr_workgroup_info 0
		.amdhsa_system_vgpr_workitem_id 0
		.amdhsa_next_free_vgpr 92
		.amdhsa_next_free_sgpr 10
		.amdhsa_accum_offset 92
		.amdhsa_reserve_vcc 1
		.amdhsa_float_round_mode_32 0
		.amdhsa_float_round_mode_16_64 0
		.amdhsa_float_denorm_mode_32 3
		.amdhsa_float_denorm_mode_16_64 3
		.amdhsa_dx10_clamp 1
		.amdhsa_ieee_mode 1
		.amdhsa_fp16_overflow 0
		.amdhsa_tg_split 0
		.amdhsa_exception_fp_ieee_invalid_op 0
		.amdhsa_exception_fp_denorm_src 0
		.amdhsa_exception_fp_ieee_div_zero 0
		.amdhsa_exception_fp_ieee_overflow 0
		.amdhsa_exception_fp_ieee_underflow 0
		.amdhsa_exception_fp_ieee_inexact 0
		.amdhsa_exception_int_div_zero 0
	.end_amdhsa_kernel

amdhsa.kernels:
  - .agpr_count:     0
    .args:
      - .actual_access:  read_only
        .address_space:  global
        .offset:         0
        .size:           8
        .value_kind:     global_buffer
      - .actual_access:  read_only
        .address_space:  global
        .offset:         8
        .size:           8
        .value_kind:     global_buffer
      - .actual_access:  read_only
        .address_space:  global
        .offset:         16
        .size:           8
        .value_kind:     global_buffer
      - .actual_access:  read_only
        .address_space:  global
        .offset:         24
        .size:           8
        .value_kind:     global_buffer
      - .actual_access:  read_only
        .address_space:  global
        .offset:         32
        .size:           8
        .value_kind:     global_buffer
      - .actual_access:  read_only
        .address_space:  global
        .offset:         40
        .size:           8
        .value_kind:     global_buffer
      - .actual_access:  write_only
        .address_space:  global
        .offset:         48
        .size:           8
        .value_kind:     global_buffer
      - .actual_access:  write_only
        .address_space:  global
        .offset:         56
        .size:           8
        .value_kind:     global_buffer
      - .actual_access:  write_only
        .address_space:  global
        .offset:         64
        .size:           8
        .value_kind:     global_buffer
      - .actual_access:  write_only
        .address_space:  global
        .offset:         72
        .size:           8
        .value_kind:     global_buffer
    .group_segment_fixed_size: 65536
    .kernarg_segment_align: 8
    .kernarg_segment_size: 80
    .language:       OpenCL C
    .language_version:
      - 2
      - 0
    .max_flat_workgroup_size: 256
    .name:           _Z11proj_kernelPKfS0_S0_S0_S0_S0_PDF16_S1_PfS2_
    .private_segment_fixed_size: 0
    .sgpr_count:     22
    .sgpr_spill_count: 0
    .symbol:         _Z11proj_kernelPKfS0_S0_S0_S0_S0_PDF16_S1_PfS2_.kd
    .uniform_work_group_size: 1
    .uses_dynamic_stack: false
    .vgpr_count:     200
    .vgpr_spill_count: 0
    .wavefront_size: 64
  - .agpr_count:     0
    .args:
      - .actual_access:  read_only
        .address_space:  global
        .offset:         0
        .size:           8
        .value_kind:     global_buffer
      - .actual_access:  write_only
        .address_space:  global
        .offset:         8
        .size:           8
        .value_kind:     global_buffer
    .group_segment_fixed_size: 12672
    .kernarg_segment_align: 8
    .kernarg_segment_size: 16
    .language:       OpenCL C
    .language_version:
      - 2
      - 0
    .max_flat_workgroup_size: 1024
    .name:           _Z12carry_kernelPKDv2_DF16_PDF16_
    .private_segment_fixed_size: 0
    .sgpr_count:     16
    .sgpr_spill_count: 0
    .symbol:         _Z12carry_kernelPKDv2_DF16_PDF16_.kd
    .uniform_work_group_size: 1
    .uses_dynamic_stack: false
    .vgpr_count:     92
    .vgpr_spill_count: 0
    .wavefront_size: 64
  - .agpr_count:     0
    .args:
      - .actual_access:  read_only
        .address_space:  global
        .offset:         0
        .size:           8
        .value_kind:     global_buffer
      - .actual_access:  read_only
        .address_space:  global
        .offset:         8
        .size:           8
        .value_kind:     global_buffer
      - .actual_access:  read_only
        .address_space:  global
        .offset:         16
        .size:           8
        .value_kind:     global_buffer
      - .actual_access:  read_only
        .address_space:  global
        .offset:         24
        .size:           8
        .value_kind:     global_buffer
      - .actual_access:  read_only
        .address_space:  global
        .offset:         32
        .size:           8
        .value_kind:     global_buffer
      - .actual_access:  write_only
        .address_space:  global
        .offset:         40
        .size:           8
        .value_kind:     global_buffer
      - .actual_access:  read_only
        .address_space:  global
        .offset:         48
        .size:           8
        .value_kind:     global_buffer
      - .actual_access:  read_only
        .address_space:  global
        .offset:         56
        .size:           8
        .value_kind:     global_buffer
    .group_segment_fixed_size: 33280
    .kernarg_segment_align: 8
    .kernarg_segment_size: 64
    .language:       OpenCL C
    .language_version:
      - 2
      - 0
    .max_flat_workgroup_size: 256
    .name:           _Z11scan_kernelILi1ELi1536ELi4EEvPKfPKDF16_S3_S1_S1_PDv2_DF16_S3_Pf
    .private_segment_fixed_size: 0
    .sgpr_count:     24
    .sgpr_spill_count: 0
    .symbol:         _Z11scan_kernelILi1ELi1536ELi4EEvPKfPKDF16_S3_S1_S1_PDv2_DF16_S3_Pf.kd
    .uniform_work_group_size: 1
    .uses_dynamic_stack: false
    .vgpr_count:     110
    .vgpr_spill_count: 0
    .wavefront_size: 64
  - .agpr_count:     0
    .args:
      - .actual_access:  read_only
        .address_space:  global
        .offset:         0
        .size:           8
        .value_kind:     global_buffer
      - .actual_access:  read_only
        .address_space:  global
        .offset:         8
        .size:           8
        .value_kind:     global_buffer
      - .actual_access:  read_only
        .address_space:  global
        .offset:         16
        .size:           8
        .value_kind:     global_buffer
      - .actual_access:  read_only
        .address_space:  global
        .offset:         24
        .size:           8
        .value_kind:     global_buffer
      - .actual_access:  read_only
        .address_space:  global
        .offset:         32
        .size:           8
        .value_kind:     global_buffer
      - .actual_access:  read_only
        .address_space:  global
        .offset:         40
        .size:           8
        .value_kind:     global_buffer
      - .actual_access:  read_only
        .address_space:  global
        .offset:         48
        .size:           8
        .value_kind:     global_buffer
      - .actual_access:  write_only
        .address_space:  global
        .offset:         56
        .size:           8
        .value_kind:     global_buffer
    .group_segment_fixed_size: 50176
    .kernarg_segment_align: 8
    .kernarg_segment_size: 64
    .language:       OpenCL C
    .language_version:
      - 2
      - 0
    .max_flat_workgroup_size: 256
    .name:           _Z11scan_kernelILi3ELi1536ELi3EEvPKfPKDF16_S3_S1_S1_PDv2_DF16_S3_Pf
    .private_segment_fixed_size: 0
    .sgpr_count:     28
    .sgpr_spill_count: 0
    .symbol:         _Z11scan_kernelILi3ELi1536ELi3EEvPKfPKDF16_S3_S1_S1_PDv2_DF16_S3_Pf.kd
    .uniform_work_group_size: 1
    .uses_dynamic_stack: false
    .vgpr_count:     168
    .vgpr_spill_count: 0
    .wavefront_size: 64
